# v18 plus: lgkmcnt(0) of the old bpermute reduction moved down to the first PV MFMA in both nca kernels
# baseline (speedup 1.0000x reference)
.LBB1_16:
	s_or_b64 exec, exec, s[2:3]
	s_movk_i32 s2, 0x168
	s_waitcnt vmcnt(4)
	v_and_b32_e32 v39, 63, v0
	v_and_b32_e32 v40, 15, v0
	v_lshlrev_b32_e32 v26, 3, v50
	v_cmp_gt_u32_e32 vcc, s2, v0
	s_and_saveexec_b64 s[2:3], vcc
	s_movk_i32 s4, 0xa0
	v_mad_u32_u24 v27, v0, s4, 0
	v_mov_b32_e32 v28, 0x3c00
	ds_write_b16 v27, v28 offset:144
	s_or_b64 exec, exec, s[2:3]
	v_lshlrev_b32_e32 v38, 2, v50
	v_or_b32_e32 v28, s21, v63
	v_add_u32_e32 v29, v28, v38
	v_sub_u32_e32 v30, v38, v61
	s_movk_i32 s7, 0x80
	v_cmp_gt_u32_e64 s[2:3], 11, v30
	v_cmp_gt_u32_e64 s[4:5], s7, v29
	v_or_b32_e32 v29, 1, v38
	s_and_b64 s[2:3], s[2:3], s[4:5]
	v_mov_b32_e32 v111, 0xff800000
	v_add_u32_e32 v30, v28, v29
	v_sub_u32_e32 v29, v29, v61
	v_cndmask_b32_e64 v112, v111, 0, s[2:3]
	v_cmp_gt_u32_e64 s[2:3], 11, v29
	v_cmp_gt_u32_e64 s[4:5], s7, v30
	v_or_b32_e32 v29, 2, v38
	v_lshrrev_b32_e32 v110, 8, v0
	s_and_b64 s[2:3], s[2:3], s[4:5]
	v_add_u32_e32 v30, v28, v29
	v_sub_u32_e32 v29, v29, v61
	v_cndmask_b32_e64 v113, v111, 0, s[2:3]
	v_cmp_gt_u32_e64 s[2:3], 11, v29
	v_or_b32_e32 v29, 3, v38
	v_mad_u32_u24 v41, v110, 7, v62
	v_cmp_gt_u32_e64 s[4:5], s7, v30
	v_add_u32_e32 v28, v28, v29
	v_mad_u32_u24 v98, v41, 20, v63
	s_and_b64 s[2:3], s[2:3], s[4:5]
	v_cmp_gt_u32_e64 s[4:5], s7, v28
	v_add_u32_e32 v28, v98, v40
	s_movk_i32 s6, 0xa0
	v_mul_lo_u32 v28, v28, s6
	v_add_u32_e32 v99, 0, v28
	v_mul_u32_u24_e32 v27, 7, v110
	v_sub_u32_e32 v29, v29, v61
	v_lshl_add_u32 v94, v26, 1, v99
	s_waitcnt lgkmcnt(0)
	s_barrier
	v_cndmask_b32_e64 v114, v111, 0, s[2:3]
	v_cmp_gt_u32_e64 s[2:3], 11, v29
	ds_read_b128 v[26:29], v94
	s_and_b64 s[2:3], s[2:3], s[4:5]
	ds_read_b128 v[34:37], v94 offset:64
	v_cndmask_b32_e64 v115, v111, 0, s[2:3]
	v_cndmask_b32_e64 v30, v111, v112, s[44:45]
	v_cndmask_b32_e64 v33, v111, v115, s[44:45]
	v_cndmask_b32_e64 v32, v111, v114, s[44:45]
	v_cndmask_b32_e64 v31, v111, v113, s[44:45]
	v_cmp_gt_u32_e32 vcc, 16, v39
	v_add_u32_e32 v98, v98, v38
	s_waitcnt lgkmcnt(1)
	v_mfma_f32_16x16x32_f16 v[30:33], v[26:29], v[10:13], v[30:33]
	ds_read_b128 v[42:45], v99 offset:128
	ds_read_b128 v[46:49], v94 offset:3200
	v_cndmask_b32_e32 v29, 0, v25, vcc
	s_waitcnt lgkmcnt(2)
	v_mfma_f32_16x16x32_f16 v[30:33], v[34:37], v[2:5], v[30:33]
	v_cndmask_b32_e32 v28, 0, v24, vcc
	v_cndmask_b32_e32 v27, 0, v23, vcc
	v_cndmask_b32_e32 v26, 0, v22, vcc
	ds_read_b128 v[34:37], v94 offset:3264
	ds_read_b128 v[50:53], v99 offset:3328
	s_waitcnt lgkmcnt(3)
	v_mfma_f32_16x16x32_f16 v[22:25], v[42:45], v[26:29], v[30:33]
	ds_read_b128 v[42:45], v94 offset:6400
	ds_read_b128 v[62:65], v94 offset:6464
	v_or_b32_e32 v98, v98, v1
	v_cndmask_b32_e64 v30, v111, v112, s[46:47]
	v_cndmask_b32_e64 v33, v111, v115, s[46:47]
	v_cndmask_b32_e64 v32, v111, v114, s[46:47]
	v_cndmask_b32_e64 v31, v111, v113, s[46:47]
	v_mul_lo_u32 v98, v98, s6
	v_lshlrev_b32_e32 v61, 3, v61
	s_waitcnt lgkmcnt(4)
	v_mfma_f32_16x16x32_f16 v[30:33], v[46:49], v[10:13], v[30:33]
	ds_read_b128 v[46:49], v99 offset:6528
	ds_read_b128 v[66:69], v94 offset:9600
	v_add3_u32 v61, 0, v98, v61
	s_waitcnt lgkmcnt(5)
	v_mfma_f32_16x16x32_f16 v[30:33], v[34:37], v[2:5], v[30:33]
	v_cndmask_b32_e64 v34, v111, v112, s[48:49]
	v_cndmask_b32_e64 v37, v111, v115, s[48:49]
	v_cndmask_b32_e64 v36, v111, v114, s[48:49]
	v_cndmask_b32_e64 v35, v111, v113, s[48:49]
	ds_read_b128 v[70:73], v94 offset:9664
	ds_read_b128 v[74:77], v99 offset:9728
	s_waitcnt lgkmcnt(6)
	v_mfma_f32_16x16x32_f16 v[30:33], v[50:53], v[26:29], v[30:33]
	ds_read_b128 v[50:53], v94 offset:12800
	ds_read_b128 v[78:81], v94 offset:12864
	s_waitcnt lgkmcnt(7)
	v_mfma_f32_16x16x32_f16 v[34:37], v[42:45], v[10:13], v[34:37]
	ds_read_b128 v[42:45], v99 offset:12928
	ds_read_b128 v[82:85], v94 offset:16000
	s_waitcnt lgkmcnt(8)
	v_mfma_f32_16x16x32_f16 v[34:37], v[62:65], v[2:5], v[34:37]
	ds_read_b128 v[62:65], v94 offset:16064
	ds_read_b128 v[86:89], v99 offset:16128
	v_mul_u32_u24_e32 v128, 0xa0, v60
	s_waitcnt lgkmcnt(9)
	v_mfma_f32_16x16x32_f16 v[34:37], v[46:49], v[26:29], v[34:37]
	v_cndmask_b32_e64 v46, v111, v112, s[50:51]
	v_cndmask_b32_e64 v49, v111, v115, s[50:51]
	v_cndmask_b32_e64 v48, v111, v114, s[50:51]
	v_cndmask_b32_e64 v47, v111, v113, s[50:51]
	ds_read_b128 v[90:93], v94 offset:19200
	ds_read_b128 v[94:97], v94 offset:19264
	s_waitcnt lgkmcnt(10)
	v_mfma_f32_16x16x32_f16 v[46:49], v[66:69], v[10:13], v[46:49]
	ds_read_b128 v[66:69], v99 offset:19328
	ds_read_b64_tr_b16 v[100:101], v61 offset:3200
	v_lshlrev_b32_e32 v129, 1, v56
	s_waitcnt lgkmcnt(11)
	v_mfma_f32_16x16x32_f16 v[46:49], v[70:73], v[2:5], v[46:49]
	ds_read_b64_tr_b16 v[98:99], v61
	ds_read_b64_tr_b16 v[70:71], v61 offset:32
	s_waitcnt lgkmcnt(12)
	v_mfma_f32_16x16x32_f16 v[46:49], v[74:77], v[26:29], v[46:49]
	v_cndmask_b32_e64 v74, v111, v112, s[52:53]
	v_cndmask_b32_e64 v77, v111, v115, s[52:53]
	v_cndmask_b32_e64 v76, v111, v114, s[52:53]
	v_cndmask_b32_e64 v75, v111, v113, s[52:53]
	ds_read_b64_tr_b16 v[72:73], v61 offset:3232
	ds_read_b64_tr_b16 v[102:103], v61 offset:64
	s_waitcnt lgkmcnt(13)
	v_mfma_f32_16x16x32_f16 v[50:53], v[50:53], v[10:13], v[74:77]
	ds_read_b64_tr_b16 v[104:105], v61 offset:3264
	v_add3_u32 v128, 0, v128, v129
	s_movk_i32 s4, 0xe39
	ds_read_b64_tr_b16 v[74:75], v61 offset:96
	s_waitcnt lgkmcnt(14)
	v_mfma_f32_16x16x32_f16 v[50:53], v[78:81], v[2:5], v[50:53]
	ds_read_b64_tr_b16 v[76:77], v61 offset:3296
	ds_read_b64_tr_b16 v[78:79], v61 offset:128
	s_movk_i32 s5, 0xffee
	s_waitcnt lgkmcnt(14)
	v_mfma_f32_16x16x32_f16 v[42:45], v[42:45], v[26:29], v[50:53]
	ds_read_b64_tr_b16 v[80:81], v61 offset:3328
	ds_read_b64_tr_b16 v[106:107], v61 offset:6400
	v_cndmask_b32_e64 v50, v111, v112, s[54:55]
	v_cndmask_b32_e64 v53, v111, v115, s[54:55]
	v_cndmask_b32_e64 v52, v111, v114, s[54:55]
	v_cndmask_b32_e64 v51, v111, v113, s[54:55]
	s_nop 0
	v_mfma_f32_16x16x32_f16 v[50:53], v[82:85], v[10:13], v[50:53]
	ds_read_b64_tr_b16 v[108:109], v61 offset:9600
	ds_read_b64_tr_b16 v[82:83], v61 offset:6432
	s_waitcnt lgkmcnt(14)
	v_mfma_f32_16x16x32_f16 v[50:53], v[62:65], v[2:5], v[50:53]
	ds_read_b64_tr_b16 v[84:85], v61 offset:9632
	ds_read_b64_tr_b16 v[62:63], v61 offset:6464
	v_mfma_f32_16x16x32_f16 v[50:53], v[86:89], v[26:29], v[50:53]
	v_cndmask_b32_e64 v86, v111, v112, s[56:57]
	v_cndmask_b32_e64 v89, v111, v115, s[56:57]
	v_cndmask_b32_e64 v88, v111, v114, s[56:57]
	v_cndmask_b32_e64 v87, v111, v113, s[56:57]
	ds_read_b64_tr_b16 v[64:65], v61 offset:9664
	ds_read_b64_tr_b16 v[110:111], v61 offset:6496
	v_mfma_f32_16x16x32_f16 v[10:13], v[90:93], v[10:13], v[86:89]
	s_mov_b32 s2, 0xff800000
	ds_read_b64_tr_b16 v[112:113], v61 offset:9696
	s_nop 0
	ds_read_b64_tr_b16 v[86:87], v61 offset:6528
	v_mfma_f32_16x16x32_f16 v[2:5], v[94:97], v[2:5], v[10:13]
	ds_read_b64_tr_b16 v[88:89], v61 offset:9728
	s_nop 1
	v_max3_f32 v12, v22, s2, v23
	v_max3_f32 v12, v12, v24, v25
	v_max3_f32 v12, v12, v30, v31
	v_max3_f32 v12, v12, v32, v33
	v_max3_f32 v12, v12, v34, v35
	v_max3_f32 v12, v12, v36, v37
	v_max3_f32 v12, v12, v46, v47
	v_max3_f32 v12, v12, v48, v49
	v_mbcnt_lo_u32_b32 v13, -1, 0
	ds_read_b64_tr_b16 v[10:11], v61 offset:12800
	s_waitcnt lgkmcnt(14)
	v_mfma_f32_16x16x32_f16 v[2:5], v[66:69], v[26:29], v[2:5]
	v_max3_f32 v12, v12, v42, v43
	v_mbcnt_hi_u32_b32 v13, -1, v13
	v_max3_f32 v12, v12, v44, v45
	v_and_b32_e32 v27, 64, v13
	v_max3_f32 v12, v12, v50, v51
	v_xor_b32_e32 v26, 16, v13
	v_add_u32_e32 v27, 64, v27
	v_max3_f32 v12, v12, v52, v53
	v_cmp_lt_i32_e32 vcc, v26, v27
	v_max3_f32 v12, v12, v2, v3
	v_max3_f32 v12, v12, v4, v5
	v_mov_b32_e32 v26, v12
	s_movk_i32 s0, 0x510
	v_permlane16_swap_b32_e32 v12, v26
	v_cmp_gt_u32_e32 vcc, 11, v41
	v_mov_b32_e32 v41, 0xc80
	v_max_f32_e32 v12, v12, v26
	v_mov_b32_e32 v13, v12
	s_nop 1
	v_permlane32_swap_b32_e32 v12, v13
	s_nop 1
	v_max_f32_e32 v26, v12, v13
	v_sub_f32_e32 v29, v34, v26
	v_exp_f32_e32 v92, v29
	v_sub_f32_e32 v29, v35, v26
	v_exp_f32_e32 v93, v29
	v_sub_f32_e32 v29, v36, v26
	v_exp_f32_e32 v36, v29
	v_sub_f32_e32 v29, v37, v26
	v_exp_f32_e32 v37, v29
	v_sub_f32_e32 v29, v46, v26
	v_exp_f32_e32 v94, v29
	v_sub_f32_e32 v29, v47, v26
	v_exp_f32_e32 v95, v29
	v_sub_f32_e32 v29, v48, v26
	v_sub_f32_e32 v13, v23, v26
	v_sub_f32_e32 v23, v25, v26
	v_sub_f32_e32 v25, v31, v26
	v_exp_f32_e32 v96, v29
	v_sub_f32_e32 v29, v49, v26
	v_sub_f32_e32 v12, v22, v26
	v_sub_f32_e32 v22, v24, v26
	v_sub_f32_e32 v24, v30, v26
	v_exp_f32_e32 v27, v25
	v_sub_f32_e32 v25, v32, v26
	v_sub_f32_e32 v28, v33, v26
	v_exp_f32_e32 v97, v29
	v_sub_f32_e32 v29, v42, v26
	v_exp_f32_e32 v12, v12
	v_exp_f32_e32 v13, v13
	v_exp_f32_e32 v22, v22
	v_exp_f32_e32 v23, v23
	v_exp_f32_e32 v24, v24
	v_exp_f32_e32 v25, v25
	v_exp_f32_e32 v28, v28
	v_exp_f32_e32 v114, v29
	v_sub_f32_e32 v29, v43, v26
	v_exp_f32_e32 v115, v29
	v_sub_f32_e32 v29, v44, v26
	v_exp_f32_e32 v116, v29
	v_sub_f32_e32 v29, v45, v26
	v_exp_f32_e32 v117, v29
	v_sub_f32_e32 v29, v50, v26
	v_exp_f32_e32 v118, v29
	v_sub_f32_e32 v29, v51, v26
	v_cvt_pk_f16_f32 v25, v25, v28
	v_cvt_pk_f16_f32 v24, v24, v27
	v_cvt_pk_f16_f32 v23, v22, v23
	v_cvt_pk_f16_f32 v22, v12, v13
	v_exp_f32_e32 v119, v29
	v_cndmask_b32_e32 v41, 0, v41, vcc
	s_waitcnt lgkmcnt(0)
	v_mfma_f32_16x16x32_f16 v[28:31], v[98:101], v[22:25], 0
	ds_read_b64_tr_b16 v[12:13], v61 offset:16000
	ds_read_b64_tr_b16 v[32:33], v61 offset:12832
	v_sub_f32_e32 v27, v52, v26
	v_mfma_f32_16x16x32_f16 v[42:45], v[70:73], v[22:25], 0
	ds_read_b64_tr_b16 v[34:35], v61 offset:16032
	ds_read_b64_tr_b16 v[46:47], v61 offset:12864
	v_exp_f32_e32 v27, v27
	v_mfma_f32_16x16x32_f16 v[66:69], v[102:105], v[22:25], 0
	ds_read_b64_tr_b16 v[48:49], v61 offset:16064
	ds_read_b64_tr_b16 v[70:71], v61 offset:12896
	v_sub_f32_e32 v2, v2, v26
	v_mfma_f32_16x16x32_f16 v[74:77], v[74:77], v[22:25], 0
	ds_read_b64_tr_b16 v[72:73], v61 offset:16096
	ds_read_b64_tr_b16 v[90:91], v61 offset:12928
	v_cmp_gt_u32_e32 vcc, s0, v58
	v_mfma_f32_16x16x32_f16 v[22:25], v[78:81], v[22:25], 0
	v_cvt_pk_f16_f32 v78, v92, v93
	ds_read_b64_tr_b16 v[92:93], v61 offset:16128
	v_cvt_pk_f16_f32 v81, v96, v97
	v_cvt_pk_f16_f32 v80, v94, v95
	v_cvt_pk_f16_f32 v79, v36, v37
	v_add_u32_e32 v36, v61, v41
	v_sub_f32_e32 v37, v53, v26
	ds_read_b64_tr_b16 v[94:95], v61 offset:19200
	v_mfma_f32_16x16x32_f16 v[28:31], v[106:109], v[78:81], v[28:31]
	ds_read_b64_tr_b16 v[96:97], v36 offset:19200
	ds_read_b64_tr_b16 v[100:101], v36 offset:19232
	v_exp_f32_e32 v37, v37
	v_mfma_f32_16x16x32_f16 v[42:45], v[82:85], v[78:81], v[42:45]
	ds_read_b64_tr_b16 v[98:99], v61 offset:19232
	ds_read_b64_tr_b16 v[50:51], v61 offset:19264
	v_mfma_f32_16x16x32_f16 v[62:65], v[62:65], v[78:81], v[66:69]
	ds_read_b64_tr_b16 v[52:53], v36 offset:19264
	s_nop 1
	ds_read_b64_tr_b16 v[66:67], v61 offset:19296
	v_mfma_f32_16x16x32_f16 v[74:77], v[110:113], v[78:81], v[74:77]
	ds_read_b64_tr_b16 v[68:69], v36 offset:19296
	ds_read_b64_tr_b16 v[82:83], v61 offset:19328
	v_mfma_f32_16x16x32_f16 v[22:25], v[86:89], v[78:81], v[22:25]
	ds_read_b64_tr_b16 v[84:85], v36 offset:19328
	s_waitcnt vmcnt(2)
	v_cvt_pk_f16_f32 v21, v20, v21
	v_cvt_pk_f16_f32 v20, v18, v19
	v_cvt_pk_f16_f32 v17, v16, v17
	v_cvt_pk_f16_f32 v16, v14, v15
	ds_write_b64 v128, v[20:21] offset:57600
	v_mul_u32_u24_sdwa v18, v59, s4 dst_sel:DWORD dst_unused:UNUSED_PAD src0_sel:WORD_0 src1_sel:DWORD
	v_mul_i32_i24_sdwa v19, v18, s5 dst_sel:DWORD dst_unused:UNUSED_PAD src0_sel:WORD_1 src1_sel:DWORD
	v_mul_u32_u24_sdwa v14, v18, s6 dst_sel:DWORD dst_unused:UNUSED_PAD src0_sel:WORD_1 src1_sel:DWORD
	v_add_lshl_u32 v15, v19, v59, 3
	v_exp_f32_e32 v18, v2
	v_sub_f32_e32 v19, v3, v26
	v_sub_f32_e32 v2, v4, v26
	v_sub_f32_e32 v21, v5, v26
	v_cvt_pk_f16_f32 v81, v27, v37
	v_cvt_pk_f16_f32 v80, v118, v119
	v_cvt_pk_f16_f32 v79, v116, v117
	v_cvt_pk_f16_f32 v78, v114, v115
	v_add3_u32 v14, 0, v14, v15
	v_exp_f32_e32 v20, v2
	v_exp_f32_e32 v21, v21
	v_exp_f32_e32 v19, v19
	s_waitcnt lgkmcnt(14)
	v_mfma_f32_16x16x32_f16 v[10:13], v[10:13], v[78:81], v[28:31]
	ds_write_b64 v14, v[16:17] offset:57600
	v_mfma_f32_16x16x32_f16 v[14:17], v[32:35], v[78:81], v[42:45]
	v_mfma_f32_16x16x32_f16 v[28:31], v[46:49], v[78:81], v[62:65]
	s_nop 1
	v_mov_b32_e32 v44, 0
	v_cvt_pk_f16_f32 v43, v20, v21
	v_cvt_pk_f16_f32 v42, v18, v19
	s_waitcnt lgkmcnt(14)
	v_mfma_f32_16x16x32_f16 v[2:5], v[70:73], v[78:81], v[74:77]
	v_mov_b32_e32 v45, v44
	s_waitcnt lgkmcnt(12)
	v_mfma_f32_16x16x32_f16 v[32:35], v[90:93], v[78:81], v[22:25]
	s_waitcnt lgkmcnt(10)
	v_mfma_f32_16x16x32_f16 v[22:25], v[94:97], v[42:45], v[10:13]
	s_waitcnt lgkmcnt(8)
	v_mfma_f32_16x16x32_f16 v[18:21], v[98:101], v[42:45], v[14:17]
	s_waitcnt lgkmcnt(6)
	v_mfma_f32_16x16x32_f16 v[14:17], v[50:53], v[42:45], v[28:31]
	s_waitcnt lgkmcnt(4)
	v_mfma_f32_16x16x32_f16 v[10:13], v[66:69], v[42:45], v[2:5]
	s_waitcnt lgkmcnt(2)
	v_mfma_f32_16x16x32_f16 v[2:5], v[82:85], v[42:45], v[32:35]
	s_and_saveexec_b64 s[0:1], vcc
	s_cbranch_execz .LBB1_20
	v_mul_u32_u24_sdwa v27, v58, s4 dst_sel:DWORD dst_unused:UNUSED_PAD src0_sel:WORD_0 src1_sel:DWORD
	v_mul_i32_i24_sdwa v28, v27, s5 dst_sel:DWORD dst_unused:UNUSED_PAD src0_sel:WORD_1 src1_sel:DWORD
	s_waitcnt vmcnt(1)
	v_cvt_pk_f16_f32 v9, v8, v9
	v_cvt_pk_f16_f32 v8, v6, v7
	v_mul_u32_u24_sdwa v6, v27, s6 dst_sel:DWORD dst_unused:UNUSED_PAD src0_sel:WORD_1 src1_sel:DWORD
	v_add_lshl_u32 v7, v28, v58, 3
	v_add3_u32 v6, 0, v6, v7
	ds_write_b64 v6, v[8:9] offset:57600
